# prologue: the fold loop (pooling maps folded into w_out) software-pipelined two deep with a second register set; rest as previous version
# speedup vs baseline: 1.0037x; 1.0037x over previous
; __global__ void __launch_bounds__(NTHR, 2) mk_fwd(Args args) {
;     ...
;                 const int i4 = r & 3, gi = (r >> 2) & 3, nb = (r >> 4) & 15, l = r >> 8, n = nb * 64 + lane;
;                 const float* wo = w_out + (size_t)l * DM * DM + (size_t)(768 + gi * 64) * DM + n;
;                 const float* __restrict__ wp = pool_w + (size_t)l * 16384 + gi * 4096; const float* __restrict__ ps = pool_scale + l * 256 + gi * 64;
;                 float v[16];
; #pragma unroll
;                 for (int i = 0; i < 16; ++i) v[i] = 0.f;
;                 for (int cp = 0; cp < 64; ++cp) { const float w = wo[(size_t)cp * DM] * ps[cp];
; #pragma unroll
;                     for (int i = 0; i < 16; ++i) v[i] += wp[(i4 * 16 + i) * 64 + cp] * w; }
.LBB0_61:
	s_andn2_b64 vcc, exec, s[22:23]
	s_cbranch_vccnz .LBB0_37
	s_ashr_i32 s22, s92, 8
	s_lshl_b32 s23, s92, 2
	s_and_b32 s93, s23, 0x3c0
	s_ashr_i32 s23, s22, 31
	s_lshl_b32 vcc_lo, s92, 16
	s_and_b32 s96, s92, 0xffffff00
	s_lshl_b64 s[94:95], s[22:23], 22
	s_and_b32 vcc_lo, vcc_lo, 0xc0000
	s_lshr_b32 s8, s92, 2
	s_lshl_b64 s[24:25], s[22:23], 16
	s_ashr_i32 s97, s96, 31
	s_or_b32 s94, s94, vcc_lo
	s_add_u32 s94, s44, s94
	v_or_b32_e32 v20, s93, v1
	s_addc_u32 s95, s45, s95
	s_lshl_b32 s93, s92, 12
	s_and_b32 s93, s93, 0xc000
	v_lshlrev_b32_e32 v130, 2, v20
	s_or_b32 s24, s24, s93
	s_and_b32 s93, s92, 3
	v_lshl_add_u64 v[10:11], s[94:95], 0, v[130:131]
	s_lshl_b32 s94, s93, 12
	s_or_b32 s24, s24, s94
	s_add_u32 s94, s12, s24
	s_addc_u32 s95, s13, s25
	s_lshl_b32 s24, s92, 6
	s_and_b32 s92, s24, 0x300
	s_lshl_b64 s[24:25], s[96:97], 2
	s_or_b32 s24, s24, s92
	s_add_u32 s92, s46, s24
	v_mov_b32_e32 v4, 0
	s_addc_u32 s96, s47, s25
	s_mov_b64 s[24:25], 0
	v_mov_b32_e32 v5, v4
	v_mov_b32_e32 v2, v4
	v_mov_b32_e32 v3, v4
	v_mov_b32_e32 v8, v4
	v_mov_b32_e32 v9, v4
	v_mov_b32_e32 v6, v4
	v_mov_b32_e32 v7, v4
	v_mov_b32_e32 v16, v4
	v_mov_b32_e32 v17, v4
	v_mov_b32_e32 v12, v4
	v_mov_b32_e32 v13, v4
	v_mov_b32_e32 v18, v4
	v_mov_b32_e32 v19, v4
	v_mov_b32_e32 v14, v4
	v_mov_b32_e32 v15, v4
	s_add_u32 vcc_lo, s92, s24
	s_addc_u32 vcc_hi, s96, s25
	global_load_dwordx2 v[22:23], v131, vcc offset:-4
	s_add_u32 vcc_lo, s94, s24
	global_load_dword v21, v[10:11], off offset:-4096
	s_addc_u32 vcc_hi, s95, s25
	global_load_dwordx2 v[24:25], v131, vcc
	global_load_dwordx2 v[26:27], v131, vcc offset:256
	global_load_dwordx2 v[28:29], v131, vcc offset:512
	global_load_dwordx2 v[30:31], v131, vcc offset:768
	global_load_dwordx2 v[32:33], v131, vcc offset:1024
	global_load_dwordx2 v[34:35], v131, vcc offset:1280
	global_load_dwordx2 v[36:37], v131, vcc offset:1536
	global_load_dwordx2 v[38:39], v131, vcc offset:1792
	global_load_dwordx2 v[40:41], v131, vcc offset:2048
	global_load_dwordx2 v[42:43], v131, vcc offset:2304
	global_load_dwordx2 v[44:45], v131, vcc offset:2560
	global_load_dwordx2 v[46:47], v131, vcc offset:2816
	global_load_dwordx2 v[48:49], v131, vcc offset:3072
	global_load_dwordx2 v[50:51], v131, vcc offset:3328
	global_load_dwordx2 v[52:53], v131, vcc offset:3584
	global_load_dwordx2 v[54:55], v131, vcc offset:3840
	global_load_dword v56, v[10:11], off
	s_add_u32 s24, s24, 8
	s_addc_u32 s25, s25, 0
	v_lshl_add_u64 v[10:11], v[10:11], 0, s[14:15]
.Lfold_loop:
	s_cmpk_eq_i32 s24, 0x100
	s_cbranch_scc1 .Lfold_lastA
	s_add_u32 vcc_lo, s92, s24
	s_addc_u32 vcc_hi, s96, s25
	global_load_dwordx2 v[142:143], v131, vcc offset:-4
	s_add_u32 vcc_lo, s94, s24
	global_load_dword v141, v[10:11], off offset:-4096
	s_addc_u32 vcc_hi, s95, s25
	global_load_dwordx2 v[144:145], v131, vcc
	global_load_dwordx2 v[146:147], v131, vcc offset:256
	global_load_dwordx2 v[148:149], v131, vcc offset:512
	global_load_dwordx2 v[150:151], v131, vcc offset:768
	global_load_dwordx2 v[152:153], v131, vcc offset:1024
	global_load_dwordx2 v[154:155], v131, vcc offset:1280
	global_load_dwordx2 v[156:157], v131, vcc offset:1536
	global_load_dwordx2 v[158:159], v131, vcc offset:1792
	global_load_dwordx2 v[160:161], v131, vcc offset:2048
	global_load_dwordx2 v[162:163], v131, vcc offset:2304
	global_load_dwordx2 v[164:165], v131, vcc offset:2560
	global_load_dwordx2 v[166:167], v131, vcc offset:2816
	global_load_dwordx2 v[168:169], v131, vcc offset:3072
	global_load_dwordx2 v[170:171], v131, vcc offset:3328
	global_load_dwordx2 v[172:173], v131, vcc offset:3584
	global_load_dwordx2 v[174:175], v131, vcc offset:3840
	global_load_dword v176, v[10:11], off
	s_add_u32 s24, s24, 8
	s_addc_u32 s25, s25, 0
	v_lshl_add_u64 v[10:11], v[10:11], 0, s[14:15]
	s_waitcnt vmcnt(35)
	v_mov_b32_e32 v58, v24
	s_waitcnt vmcnt(34)
	v_mov_b32_e32 v60, v26
	s_waitcnt vmcnt(33)
	v_mov_b32_e32 v59, v28
	s_waitcnt vmcnt(32)
	v_mov_b32_e32 v61, v30
	s_waitcnt vmcnt(31)
	v_mov_b32_e32 v62, v32
	s_waitcnt vmcnt(30)
	v_mov_b32_e32 v64, v34
	s_waitcnt vmcnt(29)
	v_mov_b32_e32 v63, v36
	s_waitcnt vmcnt(28)
	v_mov_b32_e32 v65, v38
	s_waitcnt vmcnt(27)
	v_mov_b32_e32 v66, v40
	s_waitcnt vmcnt(26)
	v_mov_b32_e32 v68, v42
	s_waitcnt vmcnt(25)
	v_mov_b32_e32 v67, v44
	s_waitcnt vmcnt(24)
	v_mov_b32_e32 v69, v46
	s_waitcnt vmcnt(23)
	v_mov_b32_e32 v70, v48
	s_waitcnt vmcnt(22)
	v_mov_b32_e32 v72, v50
	v_mul_f32_e32 v22, v21, v22
	s_waitcnt vmcnt(21)
	v_mov_b32_e32 v71, v52
	s_waitcnt vmcnt(20)
	v_mov_b32_e32 v73, v54
	s_waitcnt vmcnt(19)
	v_mul_f32_e32 v56, v56, v23
	v_mov_b32_e32 v28, v25
	v_mov_b32_e32 v30, v27
	v_mov_b32_e32 v36, v33
	v_mov_b32_e32 v38, v35
	v_mov_b32_e32 v44, v41
	v_mov_b32_e32 v46, v43
	v_mov_b32_e32 v52, v49
	v_mov_b32_e32 v54, v51
	v_pk_fma_f32 v[12:13], v[22:23], v[58:59], v[12:13] op_sel_hi:[0,1,1]
	v_pk_fma_f32 v[16:17], v[22:23], v[60:61], v[16:17] op_sel_hi:[0,1,1]
	v_pk_fma_f32 v[14:15], v[22:23], v[62:63], v[14:15] op_sel_hi:[0,1,1]
	v_pk_fma_f32 v[18:19], v[22:23], v[64:65], v[18:19] op_sel_hi:[0,1,1]
	v_pk_fma_f32 v[2:3], v[22:23], v[66:67], v[2:3] op_sel_hi:[0,1,1]
	v_pk_fma_f32 v[4:5], v[22:23], v[68:69], v[4:5] op_sel_hi:[0,1,1]
	v_pk_fma_f32 v[6:7], v[22:23], v[70:71], v[6:7] op_sel_hi:[0,1,1]
	v_pk_fma_f32 v[8:9], v[22:23], v[72:73], v[8:9] op_sel_hi:[0,1,1]
	v_pk_fma_f32 v[12:13], v[56:57], v[28:29], v[12:13] op_sel_hi:[0,1,1]
	v_pk_fma_f32 v[16:17], v[56:57], v[30:31], v[16:17] op_sel_hi:[0,1,1]
	v_pk_fma_f32 v[14:15], v[56:57], v[36:37], v[14:15] op_sel_hi:[0,1,1]
	v_pk_fma_f32 v[18:19], v[56:57], v[38:39], v[18:19] op_sel_hi:[0,1,1]
	v_pk_fma_f32 v[2:3], v[56:57], v[44:45], v[2:3] op_sel_hi:[0,1,1]
	v_pk_fma_f32 v[4:5], v[56:57], v[46:47], v[4:5] op_sel_hi:[0,1,1]
	v_pk_fma_f32 v[6:7], v[56:57], v[52:53], v[6:7] op_sel_hi:[0,1,1]
	v_pk_fma_f32 v[8:9], v[56:57], v[54:55], v[8:9] op_sel_hi:[0,1,1]
	s_cmpk_eq_i32 s24, 0x100
	s_cbranch_scc1 .Lfold_lastB
; __global__ void __launch_bounds__(NTHR, 2) mk_fwd(Args args) {
;     ...
;                 const int i4 = r & 3, gi = (r >> 2) & 3, nb = (r >> 4) & 15, l = r >> 8, n = nb * 64 + lane;
;                 const float* wo = w_out + (size_t)l * DM * DM + (size_t)(768 + gi * 64) * DM + n;
;                 const float* __restrict__ wp = pool_w + (size_t)l * 16384 + gi * 4096; const float* __restrict__ ps = pool_scale + l * 256 + gi * 64;
;                 float v[16];
; #pragma unroll
;                 for (int i = 0; i < 16; ++i) v[i] = 0.f;
;                 for (int cp = 0; cp < 64; ++cp) { const float w = wo[(size_t)cp * DM] * ps[cp];
; #pragma unroll
;                     for (int i = 0; i < 16; ++i) v[i] += wp[(i4 * 16 + i) * 64 + cp] * w; }
	s_add_u32 vcc_lo, s92, s24
	s_addc_u32 vcc_hi, s96, s25
	global_load_dwordx2 v[22:23], v131, vcc offset:-4
	s_add_u32 vcc_lo, s94, s24
	global_load_dword v21, v[10:11], off offset:-4096
	s_addc_u32 vcc_hi, s95, s25
	global_load_dwordx2 v[24:25], v131, vcc
	global_load_dwordx2 v[26:27], v131, vcc offset:256
	global_load_dwordx2 v[28:29], v131, vcc offset:512
	global_load_dwordx2 v[30:31], v131, vcc offset:768
	global_load_dwordx2 v[32:33], v131, vcc offset:1024
	global_load_dwordx2 v[34:35], v131, vcc offset:1280
	global_load_dwordx2 v[36:37], v131, vcc offset:1536
	global_load_dwordx2 v[38:39], v131, vcc offset:1792
	global_load_dwordx2 v[40:41], v131, vcc offset:2048
	global_load_dwordx2 v[42:43], v131, vcc offset:2304
	global_load_dwordx2 v[44:45], v131, vcc offset:2560
	global_load_dwordx2 v[46:47], v131, vcc offset:2816
	global_load_dwordx2 v[48:49], v131, vcc offset:3072
	global_load_dwordx2 v[50:51], v131, vcc offset:3328
	global_load_dwordx2 v[52:53], v131, vcc offset:3584
	global_load_dwordx2 v[54:55], v131, vcc offset:3840
	global_load_dword v56, v[10:11], off
	s_add_u32 s24, s24, 8
	s_addc_u32 s25, s25, 0
	v_lshl_add_u64 v[10:11], v[10:11], 0, s[14:15]
	s_waitcnt vmcnt(35)
	v_mov_b32_e32 v178, v144
	s_waitcnt vmcnt(34)
	v_mov_b32_e32 v180, v146
	s_waitcnt vmcnt(33)
	v_mov_b32_e32 v179, v148
	s_waitcnt vmcnt(32)
	v_mov_b32_e32 v181, v150
	s_waitcnt vmcnt(31)
	v_mov_b32_e32 v182, v152
	s_waitcnt vmcnt(30)
	v_mov_b32_e32 v184, v154
	s_waitcnt vmcnt(29)
	v_mov_b32_e32 v183, v156
	s_waitcnt vmcnt(28)
	v_mov_b32_e32 v185, v158
	s_waitcnt vmcnt(27)
	v_mov_b32_e32 v186, v160
	s_waitcnt vmcnt(26)
	v_mov_b32_e32 v188, v162
	s_waitcnt vmcnt(25)
	v_mov_b32_e32 v187, v164
	s_waitcnt vmcnt(24)
	v_mov_b32_e32 v189, v166
	s_waitcnt vmcnt(23)
	v_mov_b32_e32 v190, v168
	s_waitcnt vmcnt(22)
	v_mov_b32_e32 v192, v170
	v_mul_f32_e32 v142, v141, v142
	s_waitcnt vmcnt(21)
	v_mov_b32_e32 v191, v172
	s_waitcnt vmcnt(20)
	v_mov_b32_e32 v193, v174
	s_waitcnt vmcnt(19)
	v_mul_f32_e32 v176, v176, v143
	v_mov_b32_e32 v148, v145
	v_mov_b32_e32 v150, v147
	v_mov_b32_e32 v156, v153
	v_mov_b32_e32 v158, v155
	v_mov_b32_e32 v164, v161
	v_mov_b32_e32 v166, v163
	v_mov_b32_e32 v172, v169
	v_mov_b32_e32 v174, v171
	v_pk_fma_f32 v[12:13], v[142:143], v[178:179], v[12:13] op_sel_hi:[0,1,1]
	v_pk_fma_f32 v[16:17], v[142:143], v[180:181], v[16:17] op_sel_hi:[0,1,1]
	v_pk_fma_f32 v[14:15], v[142:143], v[182:183], v[14:15] op_sel_hi:[0,1,1]
	v_pk_fma_f32 v[18:19], v[142:143], v[184:185], v[18:19] op_sel_hi:[0,1,1]
	v_pk_fma_f32 v[2:3], v[142:143], v[186:187], v[2:3] op_sel_hi:[0,1,1]
	v_pk_fma_f32 v[4:5], v[142:143], v[188:189], v[4:5] op_sel_hi:[0,1,1]
	v_pk_fma_f32 v[6:7], v[142:143], v[190:191], v[6:7] op_sel_hi:[0,1,1]
	v_pk_fma_f32 v[8:9], v[142:143], v[192:193], v[8:9] op_sel_hi:[0,1,1]
	v_pk_fma_f32 v[12:13], v[176:177], v[148:149], v[12:13] op_sel_hi:[0,1,1]
	v_pk_fma_f32 v[16:17], v[176:177], v[150:151], v[16:17] op_sel_hi:[0,1,1]
	v_pk_fma_f32 v[14:15], v[176:177], v[156:157], v[14:15] op_sel_hi:[0,1,1]
	v_pk_fma_f32 v[18:19], v[176:177], v[158:159], v[18:19] op_sel_hi:[0,1,1]
	v_pk_fma_f32 v[2:3], v[176:177], v[164:165], v[2:3] op_sel_hi:[0,1,1]
	v_pk_fma_f32 v[4:5], v[176:177], v[166:167], v[4:5] op_sel_hi:[0,1,1]
	v_pk_fma_f32 v[6:7], v[176:177], v[172:173], v[6:7] op_sel_hi:[0,1,1]
	v_pk_fma_f32 v[8:9], v[176:177], v[174:175], v[8:9] op_sel_hi:[0,1,1]
	s_branch .Lfold_loop
.Lfold_lastA:
	s_waitcnt vmcnt(16)
	v_mov_b32_e32 v58, v24
	s_waitcnt vmcnt(15)
	v_mov_b32_e32 v60, v26
	s_waitcnt vmcnt(14)
	v_mov_b32_e32 v59, v28
	s_waitcnt vmcnt(13)
	v_mov_b32_e32 v61, v30
	s_waitcnt vmcnt(12)
	v_mov_b32_e32 v62, v32
	s_waitcnt vmcnt(11)
	v_mov_b32_e32 v64, v34
	s_waitcnt vmcnt(10)
	v_mov_b32_e32 v63, v36
	s_waitcnt vmcnt(9)
	v_mov_b32_e32 v65, v38
	s_waitcnt vmcnt(8)
	v_mov_b32_e32 v66, v40
	s_waitcnt vmcnt(7)
	v_mov_b32_e32 v68, v42
	s_waitcnt vmcnt(6)
	v_mov_b32_e32 v67, v44
	s_waitcnt vmcnt(5)
	v_mov_b32_e32 v69, v46
	s_waitcnt vmcnt(4)
	v_mov_b32_e32 v70, v48
	s_waitcnt vmcnt(3)
	v_mov_b32_e32 v72, v50
	v_mul_f32_e32 v22, v21, v22
	s_waitcnt vmcnt(2)
	v_mov_b32_e32 v71, v52
	s_waitcnt vmcnt(1)
	v_mov_b32_e32 v73, v54
	s_waitcnt vmcnt(0)
	v_mul_f32_e32 v56, v56, v23
	v_mov_b32_e32 v28, v25
	v_mov_b32_e32 v30, v27
	v_mov_b32_e32 v36, v33
	v_mov_b32_e32 v38, v35
	v_mov_b32_e32 v44, v41
	v_mov_b32_e32 v46, v43
	v_mov_b32_e32 v52, v49
	v_mov_b32_e32 v54, v51
	v_pk_fma_f32 v[12:13], v[22:23], v[58:59], v[12:13] op_sel_hi:[0,1,1]
	v_pk_fma_f32 v[16:17], v[22:23], v[60:61], v[16:17] op_sel_hi:[0,1,1]
	v_pk_fma_f32 v[14:15], v[22:23], v[62:63], v[14:15] op_sel_hi:[0,1,1]
	v_pk_fma_f32 v[18:19], v[22:23], v[64:65], v[18:19] op_sel_hi:[0,1,1]
	v_pk_fma_f32 v[2:3], v[22:23], v[66:67], v[2:3] op_sel_hi:[0,1,1]
	v_pk_fma_f32 v[4:5], v[22:23], v[68:69], v[4:5] op_sel_hi:[0,1,1]
	v_pk_fma_f32 v[6:7], v[22:23], v[70:71], v[6:7] op_sel_hi:[0,1,1]
	v_pk_fma_f32 v[8:9], v[22:23], v[72:73], v[8:9] op_sel_hi:[0,1,1]
	v_pk_fma_f32 v[12:13], v[56:57], v[28:29], v[12:13] op_sel_hi:[0,1,1]
	v_pk_fma_f32 v[16:17], v[56:57], v[30:31], v[16:17] op_sel_hi:[0,1,1]
	v_pk_fma_f32 v[14:15], v[56:57], v[36:37], v[14:15] op_sel_hi:[0,1,1]
	v_pk_fma_f32 v[18:19], v[56:57], v[38:39], v[18:19] op_sel_hi:[0,1,1]
	v_pk_fma_f32 v[2:3], v[56:57], v[44:45], v[2:3] op_sel_hi:[0,1,1]
	v_pk_fma_f32 v[4:5], v[56:57], v[46:47], v[4:5] op_sel_hi:[0,1,1]
	v_pk_fma_f32 v[6:7], v[56:57], v[52:53], v[6:7] op_sel_hi:[0,1,1]
	v_pk_fma_f32 v[8:9], v[56:57], v[54:55], v[8:9] op_sel_hi:[0,1,1]
	s_branch .Lfold_done
; __device__ __forceinline__ unsigned f2bf(float f) { unsigned u = __builtin_bit_cast(unsigned, f); return (u + 0x7fffu + ((u >> 16) & 1u)) >> 16; }
; __global__ void __launch_bounds__(NTHR, 2) mk_fwd(Args args) {
;     ...
;                 for (int cp = 0; cp < 64; ++cp) { const float w = wo[(size_t)cp * DM] * ps[cp];
; #pragma unroll
;                     for (int i = 0; i < 16; ++i) v[i] += wp[(i4 * 16 + i) * 64 + cp] * w; }
;                 u32x4 a, b2;
;                 a.x = f2bf(v[0]) | (f2bf(v[1]) << 16); a.y = f2bf(v[2]) | (f2bf(v[3]) << 16); a.z = f2bf(v[4]) | (f2bf(v[5]) << 16); a.w = f2bf(v[6]) | (f2bf(v[7]) << 16);
;                 b2.x = f2bf(v[8]) | (f2bf(v[9]) << 16); b2.y = f2bf(v[10]) | (f2bf(v[11]) << 16); b2.z = f2bf(v[12]) | (f2bf(v[13]) << 16); b2.w = f2bf(v[14]) | (f2bf(v[15]) << 16);
;                 u32x4* d = (u32x4*)(Wout + (size_t)l * DM * DM + (size_t)n * DM + 768 + gi * 64 + i4 * 16); d[0] = a; d[1] = b2;
.Lfold_lastB:
	s_waitcnt vmcnt(16)
	v_mov_b32_e32 v178, v144
	s_waitcnt vmcnt(15)
	v_mov_b32_e32 v180, v146
	s_waitcnt vmcnt(14)
	v_mov_b32_e32 v179, v148
	s_waitcnt vmcnt(13)
	v_mov_b32_e32 v181, v150
	s_waitcnt vmcnt(12)
	v_mov_b32_e32 v182, v152
	s_waitcnt vmcnt(11)
	v_mov_b32_e32 v184, v154
	s_waitcnt vmcnt(10)
	v_mov_b32_e32 v183, v156
	s_waitcnt vmcnt(9)
	v_mov_b32_e32 v185, v158
	s_waitcnt vmcnt(8)
	v_mov_b32_e32 v186, v160
	s_waitcnt vmcnt(7)
	v_mov_b32_e32 v188, v162
	s_waitcnt vmcnt(6)
	v_mov_b32_e32 v187, v164
	s_waitcnt vmcnt(5)
	v_mov_b32_e32 v189, v166
	s_waitcnt vmcnt(4)
	v_mov_b32_e32 v190, v168
	s_waitcnt vmcnt(3)
	v_mov_b32_e32 v192, v170
	v_mul_f32_e32 v142, v141, v142
	s_waitcnt vmcnt(2)
	v_mov_b32_e32 v191, v172
	s_waitcnt vmcnt(1)
	v_mov_b32_e32 v193, v174
	s_waitcnt vmcnt(0)
	v_mul_f32_e32 v176, v176, v143
	v_mov_b32_e32 v148, v145
	v_mov_b32_e32 v150, v147
	v_mov_b32_e32 v156, v153
	v_mov_b32_e32 v158, v155
	v_mov_b32_e32 v164, v161
	v_mov_b32_e32 v166, v163
	v_mov_b32_e32 v172, v169
	v_mov_b32_e32 v174, v171
	v_pk_fma_f32 v[12:13], v[142:143], v[178:179], v[12:13] op_sel_hi:[0,1,1]
	v_pk_fma_f32 v[16:17], v[142:143], v[180:181], v[16:17] op_sel_hi:[0,1,1]
	v_pk_fma_f32 v[14:15], v[142:143], v[182:183], v[14:15] op_sel_hi:[0,1,1]
	v_pk_fma_f32 v[18:19], v[142:143], v[184:185], v[18:19] op_sel_hi:[0,1,1]
	v_pk_fma_f32 v[2:3], v[142:143], v[186:187], v[2:3] op_sel_hi:[0,1,1]
	v_pk_fma_f32 v[4:5], v[142:143], v[188:189], v[4:5] op_sel_hi:[0,1,1]
	v_pk_fma_f32 v[6:7], v[142:143], v[190:191], v[6:7] op_sel_hi:[0,1,1]
	v_pk_fma_f32 v[8:9], v[142:143], v[192:193], v[8:9] op_sel_hi:[0,1,1]
	v_pk_fma_f32 v[12:13], v[176:177], v[148:149], v[12:13] op_sel_hi:[0,1,1]
	v_pk_fma_f32 v[16:17], v[176:177], v[150:151], v[16:17] op_sel_hi:[0,1,1]
	v_pk_fma_f32 v[14:15], v[176:177], v[156:157], v[14:15] op_sel_hi:[0,1,1]
	v_pk_fma_f32 v[18:19], v[176:177], v[158:159], v[18:19] op_sel_hi:[0,1,1]
	v_pk_fma_f32 v[2:3], v[176:177], v[164:165], v[2:3] op_sel_hi:[0,1,1]
	v_pk_fma_f32 v[4:5], v[176:177], v[166:167], v[4:5] op_sel_hi:[0,1,1]
	v_pk_fma_f32 v[6:7], v[176:177], v[172:173], v[6:7] op_sel_hi:[0,1,1]
	v_pk_fma_f32 v[8:9], v[176:177], v[174:175], v[8:9] op_sel_hi:[0,1,1]
.Lfold_done:
	v_bfe_u32 v10, v19, 16, 1
	v_bfe_u32 v11, v18, 16, 1
	v_bfe_u32 v21, v17, 16, 1
	v_bfe_u32 v22, v16, 16, 1
	v_add3_u32 v16, v16, v22, s89
	v_add3_u32 v17, v17, v21, s89
	v_add3_u32 v11, v18, v11, s89
	v_add3_u32 v10, v19, v10, s89
	v_bfe_u32 v18, v12, 16, 1
	v_bfe_u32 v19, v13, 16, 1
	v_bfe_u32 v21, v14, 16, 1
	v_bfe_u32 v22, v15, 16, 1
	v_add3_u32 v15, v15, v22, s89
	v_add3_u32 v14, v14, v21, s89
	v_add3_u32 v13, v13, v19, s89
	v_add3_u32 v12, v12, v18, s89
	v_lshrrev_b32_e32 v18, 16, v12
	v_lshrrev_b32_e32 v19, 16, v13
	v_lshrrev_b32_e32 v12, 16, v14
	v_lshrrev_b32_e32 v13, 16, v15
	v_and_or_b32 v13, v10, s90, v13
	v_and_or_b32 v12, v11, s90, v12
	v_and_or_b32 v11, v17, s90, v19
	v_and_or_b32 v10, v16, s90, v18
	v_bfe_u32 v14, v9, 16, 1
	v_bfe_u32 v15, v8, 16, 1
	v_bfe_u32 v16, v5, 16, 1
	v_bfe_u32 v17, v4, 16, 1
	s_and_b32 s8, s8, 3
	v_add3_u32 v17, v4, v17, s89
	v_add3_u32 v16, v5, v16, s89
	v_add3_u32 v4, v8, v15, s89
	v_add3_u32 v5, v9, v14, s89
	v_bfe_u32 v14, v6, 16, 1
	v_bfe_u32 v15, v7, 16, 1
	s_lshl_b64 s[22:23], s[22:23], 21
	v_add3_u32 v7, v7, v15, s89
	v_add3_u32 v6, v6, v14, s89
	s_add_u32 s22, s29, s22
	v_lshrrev_b32_e32 v6, 16, v6
	v_lshrrev_b32_e32 v7, 16, v7
	s_addc_u32 s23, s30, s23
	v_lshlrev_b32_e32 v130, 11, v20
	v_bfe_u32 v8, v2, 16, 1
	v_bfe_u32 v9, v3, 16, 1
	v_and_or_b32 v5, v5, s90, v7
	v_and_or_b32 v4, v4, s90, v6
	v_lshl_add_u64 v[6:7], s[22:23], 0, v[130:131]
	s_lshl_b32 s8, s8, 7
	v_add3_u32 v3, v3, v9, s89
	v_add3_u32 v2, v2, v8, s89
	v_lshl_add_u64 v[6:7], v[6:7], 0, s[8:9]
	s_lshl_b32 s8, s93, 5
	v_lshrrev_b32_e32 v2, 16, v2
	v_lshrrev_b32_e32 v3, 16, v3
	v_lshl_add_u64 v[6:7], v[6:7], 0, s[8:9]
	v_and_or_b32 v3, v16, s90, v3
	v_and_or_b32 v2, v17, s90, v2
	global_store_dwordx4 v[6:7], v[10:13], off offset:1536
	global_store_dwordx4 v[6:7], v[2:5], off offset:1552
	s_branch .LBB0_37
